# MoE1 epilogue: 8 serialized lrs loads batched under one wait; MoE2 epilogue: single drain instead of per-row-group vmcnt(0)
# baseline (speedup 1.0000x reference)
; __device__ __forceinline__ float fsigmoid(float x) { return __builtin_amdgcn_rcpf(1.f + __builtin_amdgcn_exp2f(-x * LOG2E)); }
;     __device__ __forceinline__ void operator()(const f32x4 (&acc)[2][2][4][2], const Unit& u, int wr, int wc, int fr, int fq) const {
;         const int row0 = u.pm * BM + wr * 64 + fr, col0 = u.pn * HALF + wc * 32 + 8 * fq; const int seg = u.a0, cnt = tab[80 + seg];
;         float rsv[2][4];
; #pragma unroll
;         for (int ai = 0; ai < 2; ++ai)
; #pragma unroll
;             for (int m = 0; m < 4; ++m) { const int rank = u.a1 * BM + ai * HALF + wr * 64 + m * 16 + fr; const float v = lrs[(size_t)seg * NTOK + (rank < cnt ? rank : 0)]; rsv[ai][m] = rank < cnt ? v : 0.f; }
; #pragma unroll
;         for (int ai = 0; ai < 2; ++ai)
; #pragma unroll
;             for (int m = 0; m < 4; ++m) { const float rs = rsv[ai][m];
;                 float r[8];
; #pragma unroll
;                 for (int n = 0; n < 2; ++n)
; #pragma unroll
;                     for (int e = 0; e < 4; ++e) { const float gt = acc[ai][0][m][n][e] * rs, up = acc[ai][1][m][n][e] * rs; r[4 * n + e] = gt * fsigmoid(gt) * up; }
.LBB0_919:
	s_lshl_b32 s19, s26, 2
	s_add_i32 s19, s19, 0
	s_add_i32 s19, s19, 0x24140
	v_mov_b32_e32 v134, s19
	ds_read_b32 v141, v134
	v_lshl_add_u32 v143, v146, 8, v137
	s_ashr_i32 s27, s26, 31
	s_lshl_b64 s[26:27], s[26:27], 18
	s_add_u32 s26, s50, s26
	s_waitcnt lgkmcnt(0)
	s_addc_u32 s27, s51, s27
	v_cmp_lt_i32_e32 vcc, v143, v141
	s_nop 1
	v_cndmask_b32_e32 v134, 0, v143, vcc
	v_ashrrev_i32_e32 v135, 31, v134
	v_lshl_add_u64 v[134:135], v[134:135], 2, s[26:27]
	global_load_dword v152, v[134:135], off
	v_or_b32_e32 v134, 16, v143
	v_cmp_lt_i32_e32 vcc, v134, v141
	s_nop 1
	v_cndmask_b32_e32 v134, 0, v134, vcc
	v_ashrrev_i32_e32 v135, 31, v134
	v_lshl_add_u64 v[134:135], v[134:135], 2, s[26:27]
	global_load_dword v148, v[134:135], off
	v_or_b32_e32 v134, 32, v143
	v_cmp_lt_i32_e32 vcc, v134, v141
	s_nop 1
	v_cndmask_b32_e32 v134, 0, v134, vcc
	v_ashrrev_i32_e32 v135, 31, v134
	v_lshl_add_u64 v[134:135], v[134:135], 2, s[26:27]
	global_load_dword v146, v[134:135], off
	v_or_b32_e32 v134, 48, v143
	v_cmp_lt_i32_e32 vcc, v134, v141
	s_nop 1
	v_cndmask_b32_e32 v134, 0, v134, vcc
	v_ashrrev_i32_e32 v135, 31, v134
	v_lshl_add_u64 v[134:135], v[134:135], 2, s[26:27]
	global_load_dword v142, v[134:135], off
	v_add_u32_e32 v134, 0x80, v143
	v_cmp_lt_i32_e32 vcc, v134, v141
	s_nop 1
	v_cndmask_b32_e32 v134, 0, v134, vcc
	v_ashrrev_i32_e32 v135, 31, v134
	v_lshl_add_u64 v[134:135], v[134:135], 2, s[26:27]
	global_load_dword v140, v[134:135], off
	v_add_u32_e32 v134, 0x90, v143
	v_cmp_lt_i32_e32 vcc, v134, v141
	s_nop 1
	v_cndmask_b32_e32 v134, 0, v134, vcc
	v_ashrrev_i32_e32 v135, 31, v134
	v_lshl_add_u64 v[134:135], v[134:135], 2, s[26:27]
	global_load_dword v138, v[134:135], off
	v_add_u32_e32 v134, 0xa0, v143
	v_cmp_lt_i32_e32 vcc, v134, v141
	s_nop 1
	v_cndmask_b32_e32 v134, 0, v134, vcc
	v_ashrrev_i32_e32 v135, 31, v134
	v_lshl_add_u64 v[134:135], v[134:135], 2, s[26:27]
	global_load_dword v136, v[134:135], off
	v_add_u32_e32 v134, 0xb0, v143
	v_cmp_lt_i32_e32 vcc, v134, v141
	s_nop 1
	v_cndmask_b32_e32 v134, 0, v134, vcc
	v_ashrrev_i32_e32 v135, 31, v134
	v_lshl_add_u64 v[134:135], v[134:135], 2, s[26:27]
	global_load_dword v134, v[134:135], off
	s_waitcnt vmcnt(0)
	v_cmp_lt_i32_e32 vcc, v143, v141
	s_nop 1
	v_cndmask_b32_e32 v152, 0, v152, vcc
	v_or_b32_e32 v135, 16, v143
	v_cmp_lt_i32_e32 vcc, v135, v141
	s_nop 1
	v_cndmask_b32_e32 v148, 0, v148, vcc
	v_or_b32_e32 v135, 32, v143
	v_cmp_lt_i32_e32 vcc, v135, v141
	s_nop 1
	v_cndmask_b32_e32 v146, 0, v146, vcc
	v_or_b32_e32 v135, 48, v143
	v_cmp_lt_i32_e32 vcc, v135, v141
	s_nop 1
	v_cndmask_b32_e32 v142, 0, v142, vcc
	v_add_u32_e32 v135, 0x80, v143
	v_cmp_lt_i32_e32 vcc, v135, v141
	s_nop 1
	v_cndmask_b32_e32 v140, 0, v140, vcc
	v_add_u32_e32 v135, 0x90, v143
	v_cmp_lt_i32_e32 vcc, v135, v141
	s_nop 1
	v_cndmask_b32_e32 v138, 0, v138, vcc
	v_add_u32_e32 v135, 0xa0, v143
	v_cmp_lt_i32_e32 vcc, v135, v141
	s_nop 1
	v_cndmask_b32_e32 v136, 0, v136, vcc
	v_add_u32_e32 v135, 0xb0, v143
	v_cmp_lt_i32_e32 vcc, v135, v141
	s_nop 1
	v_cndmask_b32_e32 v134, 0, v134, vcc
	v_lshl_add_u32 v144, s56, 8, v137
	v_lshl_or_b32 v150, s24, 7, v155
	v_ashrrev_i32_e32 v145, 31, v144
	v_ashrrev_i32_e32 v151, 31, v150
	s_mov_b32 s19, 0x20000
	s_mov_b64 s[24:25], -1
	s_mov_b32 s58, 0x358637bd
	s_nop 1
	v_pk_mul_f32 v[126:127], v[126:127], v[152:153] op_sel_hi:[1,0]
	v_pk_mul_f32 v[122:123], v[122:123], v[152:153] op_sel_hi:[1,0]
	s_nop 1
	v_pk_mul_f32 v[124:125], v[124:125], v[152:153] op_sel_hi:[1,0]
	v_pk_mul_f32 v[118:119], v[118:119], v[152:153] op_sel_hi:[1,0]
	v_pk_mul_f32 v[114:115], v[114:115], v[152:153] op_sel_hi:[1,0]
	v_pk_mul_f32 v[116:117], v[116:117], v[152:153] op_sel_hi:[1,0]
	s_nop 1
	v_pk_mul_f32 v[110:111], v[110:111], v[148:149] op_sel_hi:[1,0]
	v_pk_mul_f32 v[106:107], v[106:107], v[148:149] op_sel_hi:[1,0]
	s_nop 1
	v_pk_mul_f32 v[108:109], v[108:109], v[148:149] op_sel_hi:[1,0]
	v_pk_mul_f32 v[102:103], v[102:103], v[148:149] op_sel_hi:[1,0]
	v_pk_mul_f32 v[98:99], v[98:99], v[148:149] op_sel_hi:[1,0]
	v_pk_mul_f32 v[100:101], v[100:101], v[148:149] op_sel_hi:[1,0]
	s_nop 1
	v_pk_mul_f32 v[94:95], v[94:95], v[146:147] op_sel_hi:[1,0]
	v_pk_mul_f32 v[90:91], v[90:91], v[146:147] op_sel_hi:[1,0]
	s_nop 1
	v_pk_mul_f32 v[92:93], v[92:93], v[146:147] op_sel_hi:[1,0]
	v_pk_mul_f32 v[86:87], v[86:87], v[146:147] op_sel_hi:[1,0]
	v_pk_mul_f32 v[82:83], v[82:83], v[146:147] op_sel_hi:[1,0]
	v_pk_mul_f32 v[84:85], v[84:85], v[146:147] op_sel_hi:[1,0]
	s_nop 1
	v_pk_mul_f32 v[78:79], v[78:79], v[142:143] op_sel_hi:[1,0]
	v_pk_mul_f32 v[74:75], v[74:75], v[142:143] op_sel_hi:[1,0]
	s_nop 1
	v_pk_mul_f32 v[76:77], v[76:77], v[142:143] op_sel_hi:[1,0]
	v_pk_mul_f32 v[70:71], v[70:71], v[142:143] op_sel_hi:[1,0]
	v_pk_mul_f32 v[66:67], v[66:67], v[142:143] op_sel_hi:[1,0]
	v_pk_mul_f32 v[68:69], v[68:69], v[142:143] op_sel_hi:[1,0]
	s_nop 1
	v_pk_mul_f32 v[62:63], v[62:63], v[140:141] op_sel_hi:[1,0]
	v_pk_mul_f32 v[58:59], v[58:59], v[140:141] op_sel_hi:[1,0]
	s_nop 1
	v_pk_mul_f32 v[60:61], v[60:61], v[140:141] op_sel_hi:[1,0]
	v_pk_mul_f32 v[54:55], v[54:55], v[140:141] op_sel_hi:[1,0]
	v_pk_mul_f32 v[50:51], v[50:51], v[140:141] op_sel_hi:[1,0]
	v_pk_mul_f32 v[52:53], v[52:53], v[140:141] op_sel_hi:[1,0]
	s_nop 1
	v_pk_mul_f32 v[46:47], v[46:47], v[138:139] op_sel_hi:[1,0]
	v_pk_mul_f32 v[42:43], v[42:43], v[138:139] op_sel_hi:[1,0]
	s_nop 1
	v_pk_mul_f32 v[44:45], v[44:45], v[138:139] op_sel_hi:[1,0]
	v_pk_mul_f32 v[38:39], v[38:39], v[138:139] op_sel_hi:[1,0]
	v_pk_mul_f32 v[34:35], v[34:35], v[138:139] op_sel_hi:[1,0]
	v_pk_mul_f32 v[36:37], v[36:37], v[138:139] op_sel_hi:[1,0]
	s_nop 1
; __device__ __forceinline__ float fsigmoid(float x) { return __builtin_amdgcn_rcpf(1.f + __builtin_amdgcn_exp2f(-x * LOG2E)); }
; __device__ __forceinline__ unsigned cvt_pk_bf16(float lo, float hi) { return pk2(lo, hi); }
;     __device__ __forceinline__ void operator()(const f32x4 (&acc)[2][2][4][2], const Unit& u, int wr, int wc, int fr, int fq) const {
;     ...
;             for (int m = 0; m < 4; ++m) { const int rank = u.a1 * BM + ai * HALF + wr * 64 + m * 16 + fr; const float v = lrs[(size_t)seg * NTOK + (rank < cnt ? rank : 0)]; rsv[ai][m] = rank < cnt ? v : 0.f; }
; #pragma unroll
;         for (int ai = 0; ai < 2; ++ai)
; #pragma unroll
;             for (int m = 0; m < 4; ++m) { const float rs = rsv[ai][m];
;                 float r[8];
; #pragma unroll
;                 for (int n = 0; n < 2; ++n)
; #pragma unroll
;                     for (int e = 0; e < 4; ++e) { const float gt = acc[ai][0][m][n][e] * rs, up = acc[ai][1][m][n][e] * rs; r[4 * n + e] = gt * fsigmoid(gt) * up; }
;                 u32x4 w; w.x = cvt_pk_bf16(r[0], r[1]); w.y = cvt_pk_bf16(r[2], r[3]); w.z = cvt_pk_bf16(r[4], r[5]); w.w = cvt_pk_bf16(r[6], r[7]);
;                 *(u32x4*)(Hd + (size_t)(row0 + ai * HALF + m * 16) * DEXP + col0) = w; }
	v_pk_mul_f32 v[26:27], v[26:27], v[136:137] op_sel_hi:[1,0]
	v_pk_mul_f32 v[30:31], v[30:31], v[136:137] op_sel_hi:[1,0]
	s_nop 1
	v_mul_f32_e32 v135, 0xbfb8aa3b, v126
	v_exp_f32_e32 v135, v135
	v_pk_mul_f32 v[28:29], v[28:29], v[136:137] op_sel_hi:[1,0]
	v_pk_mul_f32 v[18:19], v[18:19], v[136:137] op_sel_hi:[1,0]
	v_pk_mul_f32 v[22:23], v[22:23], v[136:137] op_sel_hi:[1,0]
	v_add_f32_e32 v135, 1.0, v135
	v_rcp_f32_e32 v162, v135
	v_mul_f32_e32 v135, 0xbfb8aa3b, v127
	v_exp_f32_e32 v135, v135
	v_pk_mul_f32 v[32:33], v[32:33], v[136:137] op_sel_hi:[1,0]
	v_pk_mul_f32 v[24:25], v[24:25], v[136:137] op_sel_hi:[1,0]
	v_add_f32_e32 v135, 1.0, v135
	v_rcp_f32_e32 v163, v135
	s_nop 1
	v_pk_mul_f32 v[126:127], v[126:127], v[162:163]
	v_pk_mul_f32 v[10:11], v[10:11], v[134:135] op_sel_hi:[1,0]
	v_pk_mul_f32 v[122:123], v[122:123], v[126:127]
	v_pk_mul_f32 v[126:127], v[128:129], v[152:153] op_sel_hi:[1,0]
	v_pk_mul_f32 v[14:15], v[14:15], v[134:135] op_sel_hi:[1,0]
	v_mul_f32_e32 v128, 0xbfb8aa3b, v126
	v_mul_f32_e32 v129, 0xbfb8aa3b, v127
	v_exp_f32_e32 v128, v128
	v_exp_f32_e32 v129, v129
	v_pk_mul_f32 v[12:13], v[12:13], v[134:135] op_sel_hi:[1,0]
	v_pk_mul_f32 v[2:3], v[2:3], v[134:135] op_sel_hi:[1,0]
	v_add_f32_e32 v128, 1.0, v128
	v_add_f32_e32 v129, 1.0, v129
	v_rcp_f32_e32 v128, v128
	v_rcp_f32_e32 v129, v129
	v_pk_mul_f32 v[6:7], v[6:7], v[134:135] op_sel_hi:[1,0]
	v_pk_mul_f32 v[16:17], v[16:17], v[134:135] op_sel_hi:[1,0]
	v_pk_mul_f32 v[8:9], v[8:9], v[134:135] op_sel_hi:[1,0]
	v_pk_mul_f32 v[126:127], v[126:127], v[128:129]
	s_nop 0
	v_pk_mul_f32 v[124:125], v[124:125], v[126:127]
	v_mul_f32_e32 v126, 0xbfb8aa3b, v118
	v_mul_f32_e32 v127, 0xbfb8aa3b, v119
	v_exp_f32_e32 v126, v126
	v_exp_f32_e32 v127, v127
	v_add_f32_e32 v126, 1.0, v126
	v_add_f32_e32 v127, 1.0, v127
	v_rcp_f32_e32 v126, v126
	v_rcp_f32_e32 v127, v127
	s_nop 0
	v_pk_mul_f32 v[118:119], v[118:119], v[126:127]
	s_nop 0
	v_pk_mul_f32 v[114:115], v[114:115], v[118:119]
	v_pk_mul_f32 v[118:119], v[120:121], v[152:153] op_sel_hi:[1,0]
	s_nop 0
	v_mul_f32_e32 v120, 0xbfb8aa3b, v118
	v_mul_f32_e32 v121, 0xbfb8aa3b, v119
	v_exp_f32_e32 v120, v120
	v_exp_f32_e32 v121, v121
	v_add_f32_e32 v120, 1.0, v120
	v_add_f32_e32 v121, 1.0, v121
	v_rcp_f32_e32 v120, v120
	v_rcp_f32_e32 v121, v121
	s_nop 0
	v_pk_mul_f32 v[118:119], v[118:119], v[120:121]
	s_nop 0
	v_pk_mul_f32 v[116:117], v[116:117], v[118:119]
	v_cvt_pk_bf16_f32 v120, v114, v115
	v_lshlrev_b64 v[114:115], 10, v[144:145]
	v_cvt_pk_bf16_f32 v121, v116, v117
	v_lshl_add_u64 v[114:115], s[12:13], 0, v[114:115]
	v_lshlrev_b64 v[116:117], 1, v[150:151]
	v_cvt_pk_bf16_f32 v118, v122, v123
	v_cvt_pk_bf16_f32 v119, v124, v125
	v_lshl_add_u64 v[114:115], v[114:115], 0, v[116:117]
	global_store_dwordx4 v[114:115], v[118:121], off
	s_nop 1
	v_mul_f32_e32 v118, 0xbfb8aa3b, v110
	v_mul_f32_e32 v119, 0xbfb8aa3b, v111
	v_exp_f32_e32 v118, v118
	v_exp_f32_e32 v119, v119
	v_add_f32_e32 v118, 1.0, v118
	v_add_f32_e32 v119, 1.0, v119
	v_rcp_f32_e32 v118, v118
	v_rcp_f32_e32 v119, v119
	s_nop 0
	v_pk_mul_f32 v[110:111], v[110:111], v[118:119]
	s_nop 0
	v_pk_mul_f32 v[106:107], v[106:107], v[110:111]
	v_pk_mul_f32 v[110:111], v[112:113], v[148:149] op_sel_hi:[1,0]
	s_nop 0
	v_mul_f32_e32 v112, 0xbfb8aa3b, v110
	v_mul_f32_e32 v113, 0xbfb8aa3b, v111
	v_exp_f32_e32 v112, v112
	v_exp_f32_e32 v113, v113
	v_add_f32_e32 v112, 1.0, v112
	v_add_f32_e32 v113, 1.0, v113
	v_rcp_f32_e32 v112, v112
	v_rcp_f32_e32 v113, v113
	s_nop 0
	v_pk_mul_f32 v[110:111], v[110:111], v[112:113]
	s_nop 0
	v_pk_mul_f32 v[108:109], v[108:109], v[110:111]
	v_mul_f32_e32 v110, 0xbfb8aa3b, v102
	v_mul_f32_e32 v111, 0xbfb8aa3b, v103
	v_exp_f32_e32 v110, v110
	v_exp_f32_e32 v111, v111
	v_add_f32_e32 v110, 1.0, v110
	v_add_f32_e32 v111, 1.0, v111
	v_rcp_f32_e32 v110, v110
	v_rcp_f32_e32 v111, v111
	s_nop 0
	v_pk_mul_f32 v[102:103], v[102:103], v[110:111]
	s_nop 0
	v_pk_mul_f32 v[102:103], v[98:99], v[102:103]
	v_pk_mul_f32 v[98:99], v[104:105], v[148:149] op_sel_hi:[1,0]
	s_nop 0
	v_mul_f32_e32 v104, 0xbfb8aa3b, v98
	v_mul_f32_e32 v105, 0xbfb8aa3b, v99
	v_exp_f32_e32 v104, v104
	v_exp_f32_e32 v105, v105
	v_add_f32_e32 v104, 1.0, v104
	v_add_f32_e32 v105, 1.0, v105
	v_rcp_f32_e32 v104, v104
	v_rcp_f32_e32 v105, v105
	s_nop 0
	v_pk_mul_f32 v[98:99], v[98:99], v[104:105]
	s_nop 0
	v_pk_mul_f32 v[104:105], v[100:101], v[98:99]
	v_cvt_pk_bf16_f32 v100, v102, v103
	v_or_b32_e32 v102, 16, v144
	v_ashrrev_i32_e32 v103, 31, v102
	v_lshlrev_b64 v[102:103], 10, v[102:103]
	v_lshl_add_u64 v[102:103], s[12:13], 0, v[102:103]
	v_cvt_pk_bf16_f32 v98, v106, v107
	v_cvt_pk_bf16_f32 v99, v108, v109
	v_cvt_pk_bf16_f32 v101, v104, v105
	v_lshl_add_u64 v[102:103], v[102:103], 0, v[116:117]
	global_store_dwordx4 v[102:103], v[98:101], off
	s_nop 1
	v_mul_f32_e32 v98, 0xbfb8aa3b, v94
	v_mul_f32_e32 v99, 0xbfb8aa3b, v95
	v_exp_f32_e32 v98, v98
	v_exp_f32_e32 v99, v99
	v_add_f32_e32 v98, 1.0, v98
	v_add_f32_e32 v99, 1.0, v99
	v_rcp_f32_e32 v98, v98
	v_rcp_f32_e32 v99, v99
	s_nop 0
	v_pk_mul_f32 v[94:95], v[94:95], v[98:99]
	s_nop 0
	v_pk_mul_f32 v[90:91], v[90:91], v[94:95]
	v_pk_mul_f32 v[94:95], v[96:97], v[146:147] op_sel_hi:[1,0]
	s_nop 0
	v_mul_f32_e32 v96, 0xbfb8aa3b, v94
	v_mul_f32_e32 v97, 0xbfb8aa3b, v95
	v_exp_f32_e32 v96, v96
	v_exp_f32_e32 v97, v97
	v_add_f32_e32 v96, 1.0, v96
	v_add_f32_e32 v97, 1.0, v97
	v_rcp_f32_e32 v96, v96
	v_rcp_f32_e32 v97, v97
	s_nop 0
	v_pk_mul_f32 v[94:95], v[94:95], v[96:97]
	s_nop 0
	v_pk_mul_f32 v[92:93], v[92:93], v[94:95]
	v_mul_f32_e32 v94, 0xbfb8aa3b, v86
	v_mul_f32_e32 v95, 0xbfb8aa3b, v87
	v_exp_f32_e32 v94, v94
	v_exp_f32_e32 v95, v95
	v_add_f32_e32 v94, 1.0, v94
; __device__ __forceinline__ float fsigmoid(float x) { return __builtin_amdgcn_rcpf(1.f + __builtin_amdgcn_exp2f(-x * LOG2E)); }
; __device__ __forceinline__ unsigned cvt_pk_bf16(float lo, float hi) { return pk2(lo, hi); }
;     __device__ __forceinline__ void operator()(const f32x4 (&acc)[2][2][4][2], const Unit& u, int wr, int wc, int fr, int fq) const {
;     ...
;             for (int m = 0; m < 4; ++m) { const float rs = rsv[ai][m];
;                 float r[8];
; #pragma unroll
;                 for (int n = 0; n < 2; ++n)
; #pragma unroll
;                     for (int e = 0; e < 4; ++e) { const float gt = acc[ai][0][m][n][e] * rs, up = acc[ai][1][m][n][e] * rs; r[4 * n + e] = gt * fsigmoid(gt) * up; }
;                 u32x4 w; w.x = cvt_pk_bf16(r[0], r[1]); w.y = cvt_pk_bf16(r[2], r[3]); w.z = cvt_pk_bf16(r[4], r[5]); w.w = cvt_pk_bf16(r[6], r[7]);
;                 *(u32x4*)(Hd + (size_t)(row0 + ai * HALF + m * 16) * DEXP + col0) = w; }
	v_add_f32_e32 v95, 1.0, v95
	v_rcp_f32_e32 v94, v94
	v_rcp_f32_e32 v95, v95
	s_nop 0
	v_pk_mul_f32 v[86:87], v[86:87], v[94:95]
	s_nop 0
	v_pk_mul_f32 v[86:87], v[82:83], v[86:87]
	v_pk_mul_f32 v[82:83], v[88:89], v[146:147] op_sel_hi:[1,0]
	s_nop 0
	v_mul_f32_e32 v88, 0xbfb8aa3b, v82
	v_mul_f32_e32 v89, 0xbfb8aa3b, v83
	v_exp_f32_e32 v88, v88
	v_exp_f32_e32 v89, v89
	v_add_f32_e32 v88, 1.0, v88
	v_add_f32_e32 v89, 1.0, v89
	v_rcp_f32_e32 v88, v88
	v_rcp_f32_e32 v89, v89
	s_nop 0
	v_pk_mul_f32 v[82:83], v[82:83], v[88:89]
	s_nop 0
	v_pk_mul_f32 v[88:89], v[84:85], v[82:83]
	v_cvt_pk_bf16_f32 v84, v86, v87
	v_or_b32_e32 v86, 32, v144
	v_ashrrev_i32_e32 v87, 31, v86
	v_lshlrev_b64 v[86:87], 10, v[86:87]
	v_lshl_add_u64 v[86:87], s[12:13], 0, v[86:87]
	v_cvt_pk_bf16_f32 v82, v90, v91
	v_cvt_pk_bf16_f32 v83, v92, v93
	v_cvt_pk_bf16_f32 v85, v88, v89
	v_lshl_add_u64 v[86:87], v[86:87], 0, v[116:117]
	global_store_dwordx4 v[86:87], v[82:85], off
	s_nop 1
	v_mul_f32_e32 v82, 0xbfb8aa3b, v78
	v_mul_f32_e32 v83, 0xbfb8aa3b, v79
	v_exp_f32_e32 v82, v82
	v_exp_f32_e32 v83, v83
	v_add_f32_e32 v82, 1.0, v82
	v_add_f32_e32 v83, 1.0, v83
	v_rcp_f32_e32 v82, v82
	v_rcp_f32_e32 v83, v83
	s_nop 0
	v_pk_mul_f32 v[78:79], v[78:79], v[82:83]
	s_nop 0
	v_pk_mul_f32 v[74:75], v[74:75], v[78:79]
	v_pk_mul_f32 v[78:79], v[80:81], v[142:143] op_sel_hi:[1,0]
	s_nop 0
	v_mul_f32_e32 v80, 0xbfb8aa3b, v78
	v_mul_f32_e32 v81, 0xbfb8aa3b, v79
	v_exp_f32_e32 v80, v80
	v_exp_f32_e32 v81, v81
	v_add_f32_e32 v80, 1.0, v80
	v_add_f32_e32 v81, 1.0, v81
	v_rcp_f32_e32 v80, v80
	v_rcp_f32_e32 v81, v81
	s_nop 0
	v_pk_mul_f32 v[78:79], v[78:79], v[80:81]
	s_nop 0
	v_pk_mul_f32 v[76:77], v[76:77], v[78:79]
	v_mul_f32_e32 v78, 0xbfb8aa3b, v70
	v_mul_f32_e32 v79, 0xbfb8aa3b, v71
	v_exp_f32_e32 v78, v78
	v_exp_f32_e32 v79, v79
	v_add_f32_e32 v78, 1.0, v78
	v_add_f32_e32 v79, 1.0, v79
	v_rcp_f32_e32 v78, v78
	v_rcp_f32_e32 v79, v79
	s_nop 0
	v_pk_mul_f32 v[70:71], v[70:71], v[78:79]
	s_nop 0
	v_pk_mul_f32 v[70:71], v[66:67], v[70:71]
	v_pk_mul_f32 v[66:67], v[72:73], v[142:143] op_sel_hi:[1,0]
	s_nop 0
	v_mul_f32_e32 v72, 0xbfb8aa3b, v66
	v_mul_f32_e32 v73, 0xbfb8aa3b, v67
	v_exp_f32_e32 v72, v72
	v_exp_f32_e32 v73, v73
	v_add_f32_e32 v72, 1.0, v72
	v_add_f32_e32 v73, 1.0, v73
	v_rcp_f32_e32 v72, v72
	v_rcp_f32_e32 v73, v73
	s_nop 0
	v_pk_mul_f32 v[66:67], v[66:67], v[72:73]
	s_nop 0
	v_pk_mul_f32 v[72:73], v[68:69], v[66:67]
	v_cvt_pk_bf16_f32 v68, v70, v71
	v_or_b32_e32 v70, 48, v144
	v_ashrrev_i32_e32 v71, 31, v70
	v_lshlrev_b64 v[70:71], 10, v[70:71]
	v_lshl_add_u64 v[70:71], s[12:13], 0, v[70:71]
	v_cvt_pk_bf16_f32 v66, v74, v75
	v_cvt_pk_bf16_f32 v67, v76, v77
	v_cvt_pk_bf16_f32 v69, v72, v73
	v_lshl_add_u64 v[70:71], v[70:71], 0, v[116:117]
	global_store_dwordx4 v[70:71], v[66:69], off
	s_nop 1
	v_mul_f32_e32 v66, 0xbfb8aa3b, v62
	v_mul_f32_e32 v67, 0xbfb8aa3b, v63
	v_exp_f32_e32 v66, v66
	v_exp_f32_e32 v67, v67
	v_add_f32_e32 v66, 1.0, v66
	v_add_f32_e32 v67, 1.0, v67
	v_rcp_f32_e32 v66, v66
	v_rcp_f32_e32 v67, v67
	s_nop 0
	v_pk_mul_f32 v[62:63], v[62:63], v[66:67]
	s_nop 0
	v_pk_mul_f32 v[58:59], v[58:59], v[62:63]
	v_pk_mul_f32 v[62:63], v[64:65], v[140:141] op_sel_hi:[1,0]
	s_nop 0
	v_mul_f32_e32 v64, 0xbfb8aa3b, v62
	v_mul_f32_e32 v65, 0xbfb8aa3b, v63
	v_exp_f32_e32 v64, v64
	v_exp_f32_e32 v65, v65
	v_add_f32_e32 v64, 1.0, v64
	v_add_f32_e32 v65, 1.0, v65
	v_rcp_f32_e32 v64, v64
	v_rcp_f32_e32 v65, v65
	s_nop 0
	v_pk_mul_f32 v[62:63], v[62:63], v[64:65]
	s_nop 0
	v_pk_mul_f32 v[60:61], v[60:61], v[62:63]
	v_mul_f32_e32 v62, 0xbfb8aa3b, v54
	v_mul_f32_e32 v63, 0xbfb8aa3b, v55
	v_exp_f32_e32 v62, v62
	v_exp_f32_e32 v63, v63
	v_add_f32_e32 v62, 1.0, v62
	v_add_f32_e32 v63, 1.0, v63
	v_rcp_f32_e32 v62, v62
	v_rcp_f32_e32 v63, v63
	s_nop 0
	v_pk_mul_f32 v[54:55], v[54:55], v[62:63]
	s_nop 0
	v_pk_mul_f32 v[54:55], v[50:51], v[54:55]
	v_pk_mul_f32 v[50:51], v[56:57], v[140:141] op_sel_hi:[1,0]
	s_nop 0
	v_mul_f32_e32 v56, 0xbfb8aa3b, v50
	v_mul_f32_e32 v57, 0xbfb8aa3b, v51
	v_exp_f32_e32 v56, v56
	v_exp_f32_e32 v57, v57
	v_add_f32_e32 v56, 1.0, v56
	v_add_f32_e32 v57, 1.0, v57
	v_rcp_f32_e32 v56, v56
	v_rcp_f32_e32 v57, v57
	s_nop 0
	v_pk_mul_f32 v[50:51], v[50:51], v[56:57]
	s_nop 0
	v_pk_mul_f32 v[56:57], v[52:53], v[50:51]
	v_cvt_pk_bf16_f32 v52, v54, v55
	v_add_co_u32_e32 v54, vcc, s19, v114
	v_cvt_pk_bf16_f32 v50, v58, v59
	v_cvt_pk_bf16_f32 v51, v60, v61
	v_cvt_pk_bf16_f32 v53, v56, v57
	v_addc_co_u32_e32 v55, vcc, 0, v115, vcc
	global_store_dwordx4 v[54:55], v[50:53], off
	s_mov_b32 s19, 0x24000
	s_nop 0
	v_mul_f32_e32 v50, 0xbfb8aa3b, v46
	v_mul_f32_e32 v51, 0xbfb8aa3b, v47
	v_exp_f32_e32 v50, v50
	v_exp_f32_e32 v51, v51
	v_add_f32_e32 v50, 1.0, v50
	v_add_f32_e32 v51, 1.0, v51
	v_rcp_f32_e32 v50, v50
	v_rcp_f32_e32 v51, v51
	s_nop 0
	v_pk_mul_f32 v[46:47], v[46:47], v[50:51]
	s_nop 0
; __device__ __forceinline__ float fsigmoid(float x) { return __builtin_amdgcn_rcpf(1.f + __builtin_amdgcn_exp2f(-x * LOG2E)); }
; __device__ __forceinline__ unsigned cvt_pk_bf16(float lo, float hi) { return pk2(lo, hi); }
;     __device__ __forceinline__ void operator()(const f32x4 (&acc)[2][2][4][2], const Unit& u, int wr, int wc, int fr, int fq) const {
;     ...
;             for (int m = 0; m < 4; ++m) { const float rs = rsv[ai][m];
;                 float r[8];
; #pragma unroll
;                 for (int n = 0; n < 2; ++n)
; #pragma unroll
;                     for (int e = 0; e < 4; ++e) { const float gt = acc[ai][0][m][n][e] * rs, up = acc[ai][1][m][n][e] * rs; r[4 * n + e] = gt * fsigmoid(gt) * up; }
;                 u32x4 w; w.x = cvt_pk_bf16(r[0], r[1]); w.y = cvt_pk_bf16(r[2], r[3]); w.z = cvt_pk_bf16(r[4], r[5]); w.w = cvt_pk_bf16(r[6], r[7]);
;                 *(u32x4*)(Hd + (size_t)(row0 + ai * HALF + m * 16) * DEXP + col0) = w; }
	v_pk_mul_f32 v[42:43], v[42:43], v[46:47]
	v_pk_mul_f32 v[46:47], v[48:49], v[138:139] op_sel_hi:[1,0]
	s_nop 0
	v_mul_f32_e32 v48, 0xbfb8aa3b, v46
	v_mul_f32_e32 v49, 0xbfb8aa3b, v47
	v_exp_f32_e32 v48, v48
	v_exp_f32_e32 v49, v49
	v_add_f32_e32 v48, 1.0, v48
	v_add_f32_e32 v49, 1.0, v49
	v_rcp_f32_e32 v48, v48
	v_rcp_f32_e32 v49, v49
	s_nop 0
	v_pk_mul_f32 v[46:47], v[46:47], v[48:49]
	s_nop 0
	v_pk_mul_f32 v[44:45], v[44:45], v[46:47]
	v_mul_f32_e32 v46, 0xbfb8aa3b, v38
	v_mul_f32_e32 v47, 0xbfb8aa3b, v39
	v_exp_f32_e32 v46, v46
	v_exp_f32_e32 v47, v47
	v_add_f32_e32 v46, 1.0, v46
	v_add_f32_e32 v47, 1.0, v47
	v_rcp_f32_e32 v46, v46
	v_rcp_f32_e32 v47, v47
	s_nop 0
	v_pk_mul_f32 v[38:39], v[38:39], v[46:47]
	s_nop 0
	v_pk_mul_f32 v[38:39], v[34:35], v[38:39]
	v_pk_mul_f32 v[34:35], v[40:41], v[138:139] op_sel_hi:[1,0]
	s_nop 0
	v_mul_f32_e32 v40, 0xbfb8aa3b, v34
	v_mul_f32_e32 v41, 0xbfb8aa3b, v35
	v_exp_f32_e32 v40, v40
	v_exp_f32_e32 v41, v41
	v_add_f32_e32 v40, 1.0, v40
	v_add_f32_e32 v41, 1.0, v41
	v_rcp_f32_e32 v40, v40
	v_rcp_f32_e32 v41, v41
	s_nop 0
	v_pk_mul_f32 v[34:35], v[34:35], v[40:41]
	s_nop 0
	v_pk_mul_f32 v[40:41], v[36:37], v[34:35]
	v_cvt_pk_bf16_f32 v36, v38, v39
	v_add_co_u32_e32 v38, vcc, s19, v114
	v_cvt_pk_bf16_f32 v34, v42, v43
	v_cvt_pk_bf16_f32 v35, v44, v45
	v_cvt_pk_bf16_f32 v37, v40, v41
	v_addc_co_u32_e32 v39, vcc, 0, v115, vcc
	global_store_dwordx4 v[38:39], v[34:37], off
	s_mov_b32 s19, 0x28000
	s_nop 0
	v_mul_f32_e32 v34, 0xbfb8aa3b, v26
	v_mul_f32_e32 v35, 0xbfb8aa3b, v27
	v_exp_f32_e32 v34, v34
	v_exp_f32_e32 v35, v35
	v_add_f32_e32 v34, 1.0, v34
	v_add_f32_e32 v35, 1.0, v35
	v_rcp_f32_e32 v34, v34
	v_rcp_f32_e32 v35, v35
	s_nop 0
	v_pk_mul_f32 v[26:27], v[26:27], v[34:35]
	s_nop 0
	v_pk_mul_f32 v[26:27], v[30:31], v[26:27]
	v_mul_f32_e32 v30, 0xbfb8aa3b, v28
	v_mul_f32_e32 v31, 0xbfb8aa3b, v29
	v_exp_f32_e32 v30, v30
	v_exp_f32_e32 v31, v31
	v_add_f32_e32 v30, 1.0, v30
	v_add_f32_e32 v31, 1.0, v31
	v_rcp_f32_e32 v30, v30
	v_rcp_f32_e32 v31, v31
	s_nop 0
	v_pk_mul_f32 v[28:29], v[28:29], v[30:31]
	v_mul_f32_e32 v30, 0xbfb8aa3b, v18
	v_mul_f32_e32 v31, 0xbfb8aa3b, v19
	v_exp_f32_e32 v30, v30
	v_exp_f32_e32 v31, v31
	v_pk_mul_f32 v[28:29], v[32:33], v[28:29]
	v_add_f32_e32 v30, 1.0, v30
	v_add_f32_e32 v31, 1.0, v31
	v_rcp_f32_e32 v30, v30
	v_rcp_f32_e32 v31, v31
	s_nop 0
	v_pk_mul_f32 v[18:19], v[18:19], v[30:31]
	s_nop 0
	v_pk_mul_f32 v[22:23], v[22:23], v[18:19]
	v_pk_mul_f32 v[18:19], v[20:21], v[136:137] op_sel_hi:[1,0]
	s_nop 0
	v_mul_f32_e32 v20, 0xbfb8aa3b, v18
	v_mul_f32_e32 v21, 0xbfb8aa3b, v19
	v_exp_f32_e32 v20, v20
	v_exp_f32_e32 v21, v21
	v_add_f32_e32 v20, 1.0, v20
	v_add_f32_e32 v21, 1.0, v21
	v_rcp_f32_e32 v20, v20
	v_rcp_f32_e32 v21, v21
	s_nop 0
	v_pk_mul_f32 v[18:19], v[18:19], v[20:21]
	s_nop 0
	v_pk_mul_f32 v[24:25], v[24:25], v[18:19]
	v_cvt_pk_bf16_f32 v20, v22, v23
	v_add_co_u32_e32 v22, vcc, s19, v114
	v_cvt_pk_bf16_f32 v18, v26, v27
	v_cvt_pk_bf16_f32 v19, v28, v29
	v_cvt_pk_bf16_f32 v21, v24, v25
	v_addc_co_u32_e32 v23, vcc, 0, v115, vcc
	global_store_dwordx4 v[22:23], v[18:21], off
	s_nop 1
	v_mul_f32_e32 v18, 0xbfb8aa3b, v10
	v_mul_f32_e32 v19, 0xbfb8aa3b, v11
	v_exp_f32_e32 v18, v18
	v_exp_f32_e32 v19, v19
	v_add_f32_e32 v18, 1.0, v18
	v_add_f32_e32 v19, 1.0, v19
	v_rcp_f32_e32 v18, v18
	v_rcp_f32_e32 v19, v19
	s_nop 0
	v_pk_mul_f32 v[10:11], v[10:11], v[18:19]
	s_nop 0
	v_pk_mul_f32 v[10:11], v[14:15], v[10:11]
	v_mul_f32_e32 v14, 0xbfb8aa3b, v12
	v_mul_f32_e32 v15, 0xbfb8aa3b, v13
	v_exp_f32_e32 v14, v14
	v_exp_f32_e32 v15, v15
	v_add_f32_e32 v14, 1.0, v14
	v_add_f32_e32 v15, 1.0, v15
	v_rcp_f32_e32 v14, v14
	v_rcp_f32_e32 v15, v15
	s_nop 0
	v_pk_mul_f32 v[12:13], v[12:13], v[14:15]
	v_mul_f32_e32 v14, 0xbfb8aa3b, v2
	v_mul_f32_e32 v15, 0xbfb8aa3b, v3
	v_exp_f32_e32 v14, v14
	v_exp_f32_e32 v15, v15
	v_pk_mul_f32 v[12:13], v[16:17], v[12:13]
	v_add_f32_e32 v14, 1.0, v14
	v_add_f32_e32 v15, 1.0, v15
	v_rcp_f32_e32 v14, v14
	v_rcp_f32_e32 v15, v15
	s_nop 0
	v_pk_mul_f32 v[2:3], v[2:3], v[14:15]
	s_nop 0
	v_pk_mul_f32 v[6:7], v[6:7], v[2:3]
	v_pk_mul_f32 v[2:3], v[4:5], v[134:135] op_sel_hi:[1,0]
	s_nop 0
	v_mul_f32_e32 v4, 0xbfb8aa3b, v2
	v_mul_f32_e32 v5, 0xbfb8aa3b, v3
	v_exp_f32_e32 v4, v4
	v_exp_f32_e32 v5, v5
	v_add_f32_e32 v4, 1.0, v4
	v_add_f32_e32 v5, 1.0, v5
	v_rcp_f32_e32 v4, v4
	v_rcp_f32_e32 v5, v5
	s_nop 0
	v_pk_mul_f32 v[2:3], v[2:3], v[4:5]
	v_cvt_pk_bf16_f32 v4, v6, v7
	v_add_co_u32_e32 v6, vcc, 0x2c000, v114
	v_pk_mul_f32 v[8:9], v[8:9], v[2:3]
	s_nop 0
	v_addc_co_u32_e32 v7, vcc, 0, v115, vcc
	v_cvt_pk_bf16_f32 v2, v10, v11
	v_cvt_pk_bf16_f32 v3, v12, v13
	v_cvt_pk_bf16_f32 v5, v8, v9
	s_and_b64 vcc, exec, s[4:5]
	global_store_dwordx4 v[6:7], v[2:5], off
	s_cbranch_vccnz .LBB0_893
	s_andn2_b64 vcc, exec, s[10:11]
	s_cbranch_vccnz .LBB0_892
	s_barrier
	s_branch .LBB0_892

; __device__ __forceinline__ unsigned cvt_pk_bf16(float lo, float hi) { return pk2(lo, hi); }
;     __device__ __forceinline__ void operator()(const f32x4 (&acc)[2][2][4][2], const Unit& u, int wr, int wc, int fr, int fq) const {
;         const int seg = u.a0, cnt = tab[80 + seg]; bf16_t* yb = (seg >= 32) ? y1 : y0;
;         const int col0 = u.pn * BM + wc * 32 + 8 * fq;
;         int tk[2][4]; float gtv[2][4];
; #pragma unroll
;         for (int ai = 0; ai < 2; ++ai)
; #pragma unroll
;             for (int m = 0; m < 4; ++m) { const int rank = u.a1 * BM + ai * HALF + wr * 64 + m * 16 + fr; const size_t o = (size_t)seg * NTOK + (rank < cnt ? rank : 0); tk[ai][m] = ltok[o]; gtv[ai][m] = lgate[o]; }
; #pragma unroll
;         for (int ai = 0; ai < 2; ++ai)
; #pragma unroll
;             for (int m = 0; m < 4; ++m) { const int rank = u.a1 * BM + ai * HALF + wr * 64 + m * 16 + fr;
;                 if (rank < cnt) { const int tok = tk[ai][m]; const float gt = gtv[ai][m];
; #pragma unroll
;                     for (int bj = 0; bj < 2; ++bj) { const f32x4 v0 = acc[ai][bj][m][0] * gt, v1 = acc[ai][bj][m][1] * gt;
;                         u32x4 w; w.x = cvt_pk_bf16(v0[0], v0[1]); w.y = cvt_pk_bf16(v0[2], v0[3]); w.z = cvt_pk_bf16(v1[0], v1[1]); w.w = cvt_pk_bf16(v1[2], v1[3]);
;                         *(u32x4*)(yb + (size_t)tok * DM + col0 + bj * HALF) = w; } } }
.LBB0_1021:
	s_lshl_b32 s7, s6, 2
	s_add_i32 s7, s7, 0
	s_add_i32 s7, s7, 0x24140
	v_mov_b32_e32 v148, s7
	ds_read_b32 v149, v148
	v_lshlrev_b32_e32 v155, 8, v146
	s_cmp_gt_i32 s6, 31
	v_add_u32_e32 v176, v155, v1
	s_cselect_b32 s7, 0x44200000, s92
	v_or_b32_e32 v146, 16, v176
	s_add_u32 s36, s2, s7
	s_waitcnt lgkmcnt(0)
	v_cmp_lt_i32_e32 vcc, v146, v149
	s_addc_u32 s37, s3, 0
	s_ashr_i32 s7, s6, 31
	v_cndmask_b32_e32 v152, 0, v146, vcc
	s_lshl_b64 s[34:35], s[6:7], 16
	v_ashrrev_i32_e32 v153, 31, v152
	v_lshl_add_u64 v[152:153], s[34:35], 0, v[152:153]
	v_lshlrev_b64 v[152:153], 2, v[152:153]
	v_or_b32_e32 v146, 32, v176
	v_lshl_add_u64 v[158:159], s[16:17], 0, v[152:153]
	v_lshl_add_u64 v[152:153], s[18:19], 0, v[152:153]
	v_cmp_lt_i32_e32 vcc, v146, v149
	global_load_dword v174, v[158:159], off
	global_load_dword v172, v[152:153], off
	v_cndmask_b32_e32 v152, 0, v146, vcc
	v_ashrrev_i32_e32 v153, 31, v152
	v_lshl_add_u64 v[152:153], s[34:35], 0, v[152:153]
	v_lshlrev_b64 v[152:153], 2, v[152:153]
	v_or_b32_e32 v146, 48, v176
	v_lshl_add_u64 v[158:159], s[16:17], 0, v[152:153]
	v_lshl_add_u64 v[152:153], s[18:19], 0, v[152:153]
	v_cmp_lt_i32_e32 vcc, v146, v149
	global_load_dword v170, v[158:159], off
	global_load_dword v168, v[152:153], off
	v_cndmask_b32_e32 v152, 0, v146, vcc
	v_ashrrev_i32_e32 v153, 31, v152
	v_lshl_add_u64 v[152:153], s[34:35], 0, v[152:153]
	v_lshlrev_b64 v[152:153], 2, v[152:153]
	v_add_u32_e32 v146, 0x80, v176
	v_lshl_add_u64 v[158:159], s[16:17], 0, v[152:153]
	v_lshl_add_u64 v[152:153], s[18:19], 0, v[152:153]
	v_cmp_lt_i32_e64 s[10:11], v146, v149
	global_load_dword v166, v[158:159], off
	global_load_dword v164, v[152:153], off
	v_cndmask_b32_e64 v152, 0, v146, s[10:11]
	v_ashrrev_i32_e32 v153, 31, v152
	v_lshl_add_u64 v[152:153], s[34:35], 0, v[152:153]
	v_lshlrev_b64 v[152:153], 2, v[152:153]
	v_add_u32_e32 v146, 0x90, v176
	v_lshl_add_u64 v[158:159], s[16:17], 0, v[152:153]
	v_lshl_add_u64 v[152:153], s[18:19], 0, v[152:153]
	v_cmp_lt_i32_e64 s[8:9], v146, v149
	global_load_dword v162, v[158:159], off
	global_load_dword v160, v[152:153], off
	v_cndmask_b32_e64 v152, 0, v146, s[8:9]
	v_ashrrev_i32_e32 v153, 31, v152
	v_lshl_add_u64 v[152:153], s[34:35], 0, v[152:153]
	v_lshlrev_b64 v[152:153], 2, v[152:153]
	v_add_u32_e32 v146, 0xa0, v176
	v_lshl_add_u64 v[158:159], s[16:17], 0, v[152:153]
	v_lshl_add_u64 v[152:153], s[18:19], 0, v[152:153]
	v_cmp_lt_i32_e64 s[6:7], v146, v149
	global_load_dword v158, v[158:159], off
	v_cmp_lt_i32_e64 s[12:13], v176, v149
	global_load_dword v156, v[152:153], off
	v_cndmask_b32_e64 v152, 0, v146, s[6:7]
	v_ashrrev_i32_e32 v153, 31, v152
	v_lshl_add_u64 v[152:153], s[34:35], 0, v[152:153]
	v_lshlrev_b64 v[152:153], 2, v[152:153]
	v_add_u32_e32 v146, 0xb0, v176
	v_lshl_add_u64 v[178:179], s[16:17], 0, v[152:153]
	v_lshl_add_u64 v[152:153], s[18:19], 0, v[152:153]
	v_cmp_lt_i32_e32 vcc, v146, v149
	global_load_dword v154, v[178:179], off
	global_load_dword v150, v[152:153], off
	v_cndmask_b32_e32 v152, 0, v146, vcc
	v_ashrrev_i32_e32 v153, 31, v152
	v_lshl_add_u64 v[152:153], s[34:35], 0, v[152:153]
	v_lshlrev_b64 v[152:153], 2, v[152:153]
	v_lshl_add_u64 v[178:179], s[16:17], 0, v[152:153]
	v_lshl_add_u64 v[152:153], s[18:19], 0, v[152:153]
	global_load_dword v148, v[178:179], off
	global_load_dword v146, v[152:153], off
	v_lshl_or_b32 v152, s26, 8, v165
	v_ashrrev_i32_e32 v153, 31, v152
	v_lshl_add_u64 v[152:153], v[152:153], 1, s[36:37]
	s_nop 1
	v_cndmask_b32_e64 v176, 0, v176, s[12:13]
	v_ashrrev_i32_e32 v177, 31, v176
	v_lshl_add_u64 v[176:177], s[34:35], 0, v[176:177]
	v_lshlrev_b64 v[176:177], 2, v[176:177]
	v_lshl_add_u64 v[178:179], s[18:19], 0, v[176:177]
	v_lshl_add_u64 v[176:177], s[16:17], 0, v[176:177]
	global_load_dword v178, v[178:179], off
	s_nop 0
	global_load_dword v176, v[176:177], off
	s_waitcnt vmcnt(0)
	s_and_saveexec_b64 s[26:27], s[12:13]
	s_cbranch_execz .LBB0_1023
	v_pk_mul_f32 v[128:129], v[128:129], v[178:179] op_sel_hi:[1,0]
	v_pk_mul_f32 v[126:127], v[126:127], v[178:179] op_sel_hi:[1,0]
	v_ashrrev_i32_e32 v177, 31, v176
	v_lshlrev_b64 v[176:177], 11, v[176:177]
	v_pk_mul_f32 v[180:181], v[124:125], v[178:179] op_sel_hi:[1,0]
	v_pk_mul_f32 v[124:125], v[122:123], v[178:179] op_sel_hi:[1,0]
	v_lshl_add_u64 v[176:177], v[152:153], 0, v[176:177]
	v_cvt_pk_bf16_f32 v122, v126, v127
	v_cvt_pk_bf16_f32 v123, v128, v129
	v_cvt_pk_bf16_f32 v124, v124, v125
	v_cvt_pk_bf16_f32 v125, v180, v181
	global_store_dwordx4 v[176:177], v[122:125], off
	v_pk_mul_f32 v[120:121], v[120:121], v[178:179] op_sel_hi:[1,0]
	v_pk_mul_f32 v[118:119], v[118:119], v[178:179] op_sel_hi:[1,0]
	v_pk_mul_f32 v[122:123], v[116:117], v[178:179] op_sel_hi:[1,0]
	v_pk_mul_f32 v[116:117], v[114:115], v[178:179] op_sel_hi:[1,0]
	v_cvt_pk_bf16_f32 v114, v118, v119
	v_cvt_pk_bf16_f32 v115, v120, v121
	v_cvt_pk_bf16_f32 v116, v116, v117
	v_cvt_pk_bf16_f32 v117, v122, v123
	global_store_dwordx4 v[176:177], v[114:117], off offset:256
; __device__ __forceinline__ unsigned cvt_pk_bf16(float lo, float hi) { return pk2(lo, hi); }
;     __device__ __forceinline__ void operator()(const f32x4 (&acc)[2][2][4][2], const Unit& u, int wr, int wc, int fr, int fq) const {
;     ...
;             for (int m = 0; m < 4; ++m) { const int rank = u.a1 * BM + ai * HALF + wr * 64 + m * 16 + fr;
;                 if (rank < cnt) { const int tok = tk[ai][m]; const float gt = gtv[ai][m];
; #pragma unroll
;                     for (int bj = 0; bj < 2; ++bj) { const f32x4 v0 = acc[ai][bj][m][0] * gt, v1 = acc[ai][bj][m][1] * gt;
;                         u32x4 w; w.x = cvt_pk_bf16(v0[0], v0[1]); w.y = cvt_pk_bf16(v0[2], v0[3]); w.z = cvt_pk_bf16(v1[0], v1[1]); w.w = cvt_pk_bf16(v1[2], v1[3]);
;                         *(u32x4*)(yb + (size_t)tok * DM + col0 + bj * HALF) = w; } } }
.LBB0_1023:
	s_or_b64 exec, exec, s[26:27]
	s_nop 0
	v_add_u32_e32 v114, v151, v155
	v_cmp_lt_i32_e64 s[12:13], v114, v149
	s_and_saveexec_b64 s[26:27], s[12:13]
	s_mov_b64 s[36:37], 0x2000
	s_cbranch_execz .LBB0_1025
	v_ashrrev_i32_e32 v175, 31, v174
	v_lshlrev_b64 v[114:115], 11, v[174:175]
	v_pk_mul_f32 v[112:113], v[112:113], v[172:173] op_sel_hi:[1,0]
	v_pk_mul_f32 v[110:111], v[110:111], v[172:173] op_sel_hi:[1,0]
	v_pk_mul_f32 v[116:117], v[108:109], v[172:173] op_sel_hi:[1,0]
	v_pk_mul_f32 v[108:109], v[106:107], v[172:173] op_sel_hi:[1,0]
	v_lshl_add_u64 v[114:115], v[152:153], 0, v[114:115]
	v_cvt_pk_bf16_f32 v106, v110, v111
	v_cvt_pk_bf16_f32 v107, v112, v113
	v_cvt_pk_bf16_f32 v108, v108, v109
	v_cvt_pk_bf16_f32 v109, v116, v117
	global_store_dwordx4 v[114:115], v[106:109], off
	v_pk_mul_f32 v[104:105], v[104:105], v[172:173] op_sel_hi:[1,0]
	v_pk_mul_f32 v[102:103], v[102:103], v[172:173] op_sel_hi:[1,0]
	v_pk_mul_f32 v[106:107], v[100:101], v[172:173] op_sel_hi:[1,0]
	v_pk_mul_f32 v[100:101], v[98:99], v[172:173] op_sel_hi:[1,0]
	v_cvt_pk_bf16_f32 v98, v102, v103
	v_cvt_pk_bf16_f32 v99, v104, v105
	v_cvt_pk_bf16_f32 v100, v100, v101
	v_cvt_pk_bf16_f32 v101, v106, v107
	global_store_dwordx4 v[114:115], v[98:101], off offset:256
.LBB0_1025:
	s_or_b64 exec, exec, s[26:27]
	s_nop 0
	v_add_u32_e32 v98, v157, v155
	v_cmp_lt_i32_e64 s[12:13], v98, v149
	s_and_saveexec_b64 s[26:27], s[12:13]
	s_cbranch_execz .LBB0_1027
	v_ashrrev_i32_e32 v171, 31, v170
	v_lshlrev_b64 v[98:99], 11, v[170:171]
	v_pk_mul_f32 v[96:97], v[96:97], v[168:169] op_sel_hi:[1,0]
	v_pk_mul_f32 v[94:95], v[94:95], v[168:169] op_sel_hi:[1,0]
	v_pk_mul_f32 v[100:101], v[92:93], v[168:169] op_sel_hi:[1,0]
	v_pk_mul_f32 v[92:93], v[90:91], v[168:169] op_sel_hi:[1,0]
	v_lshl_add_u64 v[98:99], v[152:153], 0, v[98:99]
	v_cvt_pk_bf16_f32 v90, v94, v95
	v_cvt_pk_bf16_f32 v91, v96, v97
	v_cvt_pk_bf16_f32 v92, v92, v93
	v_cvt_pk_bf16_f32 v93, v100, v101
	global_store_dwordx4 v[98:99], v[90:93], off
	v_pk_mul_f32 v[88:89], v[88:89], v[168:169] op_sel_hi:[1,0]
	v_pk_mul_f32 v[86:87], v[86:87], v[168:169] op_sel_hi:[1,0]
	v_pk_mul_f32 v[90:91], v[84:85], v[168:169] op_sel_hi:[1,0]
	v_pk_mul_f32 v[84:85], v[82:83], v[168:169] op_sel_hi:[1,0]
	v_cvt_pk_bf16_f32 v82, v86, v87
	v_cvt_pk_bf16_f32 v83, v88, v89
	v_cvt_pk_bf16_f32 v84, v84, v85
	v_cvt_pk_bf16_f32 v85, v90, v91
	global_store_dwordx4 v[98:99], v[82:85], off offset:256

; __device__ __forceinline__ unsigned cvt_pk_bf16(float lo, float hi) { return pk2(lo, hi); }
;     __device__ __forceinline__ void operator()(const f32x4 (&acc)[2][2][4][2], const Unit& u, int wr, int wc, int fr, int fq) const {
;     ...
;             for (int m = 0; m < 4; ++m) { const int rank = u.a1 * BM + ai * HALF + wr * 64 + m * 16 + fr;
;                 if (rank < cnt) { const int tok = tk[ai][m]; const float gt = gtv[ai][m];
; #pragma unroll
;                     for (int bj = 0; bj < 2; ++bj) { const f32x4 v0 = acc[ai][bj][m][0] * gt, v1 = acc[ai][bj][m][1] * gt;
;                         u32x4 w; w.x = cvt_pk_bf16(v0[0], v0[1]); w.y = cvt_pk_bf16(v0[2], v0[3]); w.z = cvt_pk_bf16(v1[0], v1[1]); w.w = cvt_pk_bf16(v1[2], v1[3]);
;                         *(u32x4*)(yb + (size_t)tok * DM + col0 + bj * HALF) = w; } } }
.LBB0_1033:
	v_ashrrev_i32_e32 v167, 31, v166
	v_lshlrev_b64 v[82:83], 11, v[166:167]
	v_pk_mul_f32 v[80:81], v[80:81], v[164:165] op_sel_hi:[1,0]
	v_pk_mul_f32 v[78:79], v[78:79], v[164:165] op_sel_hi:[1,0]
	v_pk_mul_f32 v[84:85], v[76:77], v[164:165] op_sel_hi:[1,0]
	v_pk_mul_f32 v[76:77], v[74:75], v[164:165] op_sel_hi:[1,0]
	v_lshl_add_u64 v[82:83], v[152:153], 0, v[82:83]
	v_cvt_pk_bf16_f32 v74, v78, v79
	v_cvt_pk_bf16_f32 v75, v80, v81
	v_cvt_pk_bf16_f32 v76, v76, v77
	v_cvt_pk_bf16_f32 v77, v84, v85
	global_store_dwordx4 v[82:83], v[74:77], off
	v_pk_mul_f32 v[72:73], v[72:73], v[164:165] op_sel_hi:[1,0]
	v_pk_mul_f32 v[70:71], v[70:71], v[164:165] op_sel_hi:[1,0]
	v_pk_mul_f32 v[74:75], v[68:69], v[164:165] op_sel_hi:[1,0]
	v_pk_mul_f32 v[68:69], v[66:67], v[164:165] op_sel_hi:[1,0]
	v_cvt_pk_bf16_f32 v66, v70, v71
	v_cvt_pk_bf16_f32 v67, v72, v73
	v_cvt_pk_bf16_f32 v68, v68, v69
	v_cvt_pk_bf16_f32 v69, v74, v75
	global_store_dwordx4 v[82:83], v[66:69], off offset:256
	s_or_b64 exec, exec, s[26:27]
	s_and_saveexec_b64 s[12:13], s[10:11]
	s_cbranch_execz .LBB0_1029
.LBB0_1034:
	v_ashrrev_i32_e32 v163, 31, v162
	v_lshlrev_b64 v[66:67], 11, v[162:163]
	v_pk_mul_f32 v[64:65], v[64:65], v[160:161] op_sel_hi:[1,0]
	v_pk_mul_f32 v[62:63], v[62:63], v[160:161] op_sel_hi:[1,0]
	v_pk_mul_f32 v[68:69], v[60:61], v[160:161] op_sel_hi:[1,0]
	v_pk_mul_f32 v[60:61], v[58:59], v[160:161] op_sel_hi:[1,0]
	v_lshl_add_u64 v[66:67], v[152:153], 0, v[66:67]
	v_cvt_pk_bf16_f32 v58, v62, v63
	v_cvt_pk_bf16_f32 v59, v64, v65
	v_cvt_pk_bf16_f32 v60, v60, v61
	v_cvt_pk_bf16_f32 v61, v68, v69
	global_store_dwordx4 v[66:67], v[58:61], off
	v_pk_mul_f32 v[48:49], v[48:49], v[160:161] op_sel_hi:[1,0]
	v_pk_mul_f32 v[46:47], v[46:47], v[160:161] op_sel_hi:[1,0]
	v_pk_mul_f32 v[58:59], v[40:41], v[160:161] op_sel_hi:[1,0]
	v_pk_mul_f32 v[40:41], v[38:39], v[160:161] op_sel_hi:[1,0]
	v_cvt_pk_bf16_f32 v38, v46, v47
	v_cvt_pk_bf16_f32 v39, v48, v49
	v_cvt_pk_bf16_f32 v40, v40, v41
	v_cvt_pk_bf16_f32 v41, v58, v59
	global_store_dwordx4 v[66:67], v[38:41], off offset:256
	s_or_b64 exec, exec, s[12:13]
	s_and_saveexec_b64 s[10:11], s[8:9]
	s_cbranch_execz .LBB0_1030
.LBB0_1035:
	v_ashrrev_i32_e32 v159, 31, v158
	v_lshlrev_b64 v[38:39], 11, v[158:159]
	v_pk_mul_f32 v[40:41], v[44:45], v[156:157] op_sel_hi:[1,0]
	v_pk_mul_f32 v[42:43], v[42:43], v[156:157] op_sel_hi:[1,0]
	v_pk_mul_f32 v[44:45], v[36:37], v[156:157] op_sel_hi:[1,0]
	v_pk_mul_f32 v[36:37], v[34:35], v[156:157] op_sel_hi:[1,0]
	v_lshl_add_u64 v[38:39], v[152:153], 0, v[38:39]
	v_cvt_pk_bf16_f32 v34, v42, v43
	v_cvt_pk_bf16_f32 v35, v40, v41
	v_cvt_pk_bf16_f32 v36, v36, v37
	v_cvt_pk_bf16_f32 v37, v44, v45
	global_store_dwordx4 v[38:39], v[34:37], off
	v_pk_mul_f32 v[24:25], v[24:25], v[156:157] op_sel_hi:[1,0]
	v_pk_mul_f32 v[22:23], v[22:23], v[156:157] op_sel_hi:[1,0]
	v_pk_mul_f32 v[34:35], v[16:17], v[156:157] op_sel_hi:[1,0]
	v_pk_mul_f32 v[16:17], v[14:15], v[156:157] op_sel_hi:[1,0]
	v_cvt_pk_bf16_f32 v14, v22, v23
	v_cvt_pk_bf16_f32 v15, v24, v25
	v_cvt_pk_bf16_f32 v16, v16, v17
	v_cvt_pk_bf16_f32 v17, v34, v35
	global_store_dwordx4 v[38:39], v[14:17], off offset:256
	s_or_b64 exec, exec, s[10:11]
	s_and_saveexec_b64 s[8:9], s[6:7]
	s_cbranch_execz .LBB0_1031
.LBB0_1036:
	v_ashrrev_i32_e32 v155, 31, v154
	v_lshlrev_b64 v[14:15], 11, v[154:155]
	v_pk_mul_f32 v[16:17], v[20:21], v[150:151] op_sel_hi:[1,0]
	v_pk_mul_f32 v[18:19], v[18:19], v[150:151] op_sel_hi:[1,0]
	v_pk_mul_f32 v[20:21], v[12:13], v[150:151] op_sel_hi:[1,0]
	v_pk_mul_f32 v[12:13], v[10:11], v[150:151] op_sel_hi:[1,0]
	v_lshl_add_u64 v[14:15], v[152:153], 0, v[14:15]
	v_cvt_pk_bf16_f32 v10, v18, v19
	v_cvt_pk_bf16_f32 v11, v16, v17
	v_cvt_pk_bf16_f32 v12, v12, v13
	v_cvt_pk_bf16_f32 v13, v20, v21
	global_store_dwordx4 v[14:15], v[10:13], off
	v_pk_mul_f32 v[16:17], v[56:57], v[150:151] op_sel_hi:[1,0]
	v_pk_mul_f32 v[18:19], v[54:55], v[150:151] op_sel_hi:[1,0]
	v_pk_mul_f32 v[12:13], v[52:53], v[150:151] op_sel_hi:[1,0]
	v_pk_mul_f32 v[10:11], v[50:51], v[150:151] op_sel_hi:[1,0]
	s_nop 0
	v_cvt_pk_bf16_f32 v10, v10, v11
	v_cvt_pk_bf16_f32 v11, v12, v13
	v_cvt_pk_bf16_f32 v12, v18, v19
	v_cvt_pk_bf16_f32 v13, v16, v17
	global_store_dwordx4 v[14:15], v[10:13], off offset:256
	s_or_b64 exec, exec, s[8:9]
	s_and_saveexec_b64 s[6:7], vcc
	s_cbranch_execz .LBB0_1032
.LBB0_1037:
	v_ashrrev_i32_e32 v149, 31, v148
	v_lshlrev_b64 v[10:11], 11, v[148:149]
	v_pk_mul_f32 v[8:9], v[8:9], v[146:147] op_sel_hi:[1,0]
	v_pk_mul_f32 v[6:7], v[6:7], v[146:147] op_sel_hi:[1,0]
	v_pk_mul_f32 v[12:13], v[4:5], v[146:147] op_sel_hi:[1,0]
	v_pk_mul_f32 v[4:5], v[2:3], v[146:147] op_sel_hi:[1,0]
	v_lshl_add_u64 v[10:11], v[152:153], 0, v[10:11]
	v_cvt_pk_bf16_f32 v2, v6, v7
	v_cvt_pk_bf16_f32 v3, v8, v9
	v_cvt_pk_bf16_f32 v4, v4, v5
	v_cvt_pk_bf16_f32 v5, v12, v13
	global_store_dwordx4 v[10:11], v[2:5], off
	v_pk_mul_f32 v[6:7], v[32:33], v[146:147] op_sel_hi:[1,0]
	v_pk_mul_f32 v[8:9], v[30:31], v[146:147] op_sel_hi:[1,0]
	v_pk_mul_f32 v[4:5], v[28:29], v[146:147] op_sel_hi:[1,0]
	v_pk_mul_f32 v[2:3], v[26:27], v[146:147] op_sel_hi:[1,0]
	s_nop 0
	v_cvt_pk_bf16_f32 v2, v2, v3
	v_cvt_pk_bf16_f32 v3, v4, v5
	v_cvt_pk_bf16_f32 v4, v8, v9
	v_cvt_pk_bf16_f32 v5, v6, v7
	global_store_dwordx4 v[10:11], v[2:5], off offset:256
	s_or_b64 exec, exec, s[6:7]
	s_and_b64 vcc, exec, s[4:5]
	s_mov_b64 s[4:5], -1
	s_cbranch_vccnz .LBB0_1003
